# fp8 GEMM K-loops: the first K iteration's first-sub-phase MFMAs (out-of-line copy) take the inline constant 0 as C, so the tile header no longer zeroes any accumulator
# speedup vs baseline: 1.0071x; 1.0029x over previous
.LBB0_545:
	s_ashr_i32 s15, s14, 31
	s_lshl_b64 s[16:17], s[14:15], 18
	s_add_u32 s16, s30, s16
	s_addc_u32 s17, s31, s17
	s_and_b64 s[18:19], s[2:3], exec
	s_cselect_b32 s1, s17, s25
	s_cselect_b32 s15, s16, s24
	s_ashr_i32 s13, s12, 31
	s_lshl_b64 s[18:19], s[12:13], 18
	s_add_u32 s18, s34, s18
	s_addc_u32 s19, s35, s19
	s_and_b64 s[26:27], s[2:3], exec
	s_cselect_b32 s13, s19, s23
	s_cselect_b32 s33, s18, s22
	s_add_u32 s59, s22, 0x100
	s_addc_u32 s60, s23, 0
	s_add_u32 s22, s24, 0x80
	v_mov_b32_e32 v2, 0
	s_addc_u32 s23, s25, 0
	s_mov_b32 s61, -2
	v_mov_b32_e32 v3, v2
	s_waitcnt vmcnt(0)
	s_branch .LBB0_546
.Llzf_2:
	v_mfma_f32_16x16x128_f8f6f4 v[126:129], v[130:137], v[186:193], 0
	v_mov_b32_e32 v4, 0
	v_mov_b32_e32 v5, 0
	v_mov_b32_e32 v6, 0
	v_mov_b32_e32 v7, 0
	v_mfma_f32_16x16x128_f8f6f4 v[122:125], v[138:145], v[186:193], 0
	v_mov_b32_e32 v8, 0
	v_mov_b32_e32 v9, 0
	v_mov_b32_e32 v14, 0
	v_mov_b32_e32 v15, 0
	v_mfma_f32_16x16x128_f8f6f4 v[110:113], v[130:137], v[194:201], 0
	v_mov_b32_e32 v16, 0
	v_mov_b32_e32 v17, 0
	v_mov_b32_e32 v22, 0
	v_mov_b32_e32 v23, 0
	v_mfma_f32_16x16x128_f8f6f4 v[106:109], v[138:145], v[194:201], 0
	v_mov_b32_e32 v24, 0
	v_mov_b32_e32 v25, 0
	v_mov_b32_e32 v30, 0
	v_mov_b32_e32 v31, 0
	v_mfma_f32_16x16x128_f8f6f4 v[98:101], v[130:137], v[202:209], 0
	v_mov_b32_e32 v32, 0
	v_mov_b32_e32 v33, 0
	v_mov_b32_e32 v38, 0
	v_mov_b32_e32 v39, 0
	v_mfma_f32_16x16x128_f8f6f4 v[162:165], v[138:145], v[202:209], 0
	v_mov_b32_e32 v40, 0
	v_mov_b32_e32 v41, 0
	v_mov_b32_e32 v46, 0
	v_mov_b32_e32 v47, 0
	v_mfma_f32_16x16x128_f8f6f4 v[172:175], v[130:137], v[210:217], 0
	v_mov_b32_e32 v48, 0
	v_mov_b32_e32 v49, 0
	v_mov_b32_e32 v54, 0
	v_mov_b32_e32 v55, 0
	v_mfma_f32_16x16x128_f8f6f4 v[218:221], v[138:145], v[210:217], 0
	v_mov_b32_e32 v56, 0
	v_mov_b32_e32 v57, 0
	v_mov_b32_e32 v10, 0
	v_mov_b32_e32 v11, 0
	s_setprio 0
	s_setprio 1
	v_mfma_f32_16x16x128_f8f6f4 v[118:121], v[146:153], v[186:193], 0
	v_mov_b32_e32 v12, 0
	v_mov_b32_e32 v13, 0
	v_mov_b32_e32 v18, 0
	v_mov_b32_e32 v19, 0
	v_mfma_f32_16x16x128_f8f6f4 v[114:117], v[154:161], v[186:193], 0
	v_mov_b32_e32 v20, 0
	v_mov_b32_e32 v21, 0
	v_mov_b32_e32 v26, 0
	v_mov_b32_e32 v27, 0
	v_mfma_f32_16x16x128_f8f6f4 v[102:105], v[146:153], v[194:201], 0
	v_mov_b32_e32 v28, 0
	v_mov_b32_e32 v29, 0
	v_mov_b32_e32 v34, 0
	v_mov_b32_e32 v35, 0
	v_mfma_f32_16x16x128_f8f6f4 v[186:189], v[154:161], v[194:201], 0
	v_mov_b32_e32 v36, 0
	v_mov_b32_e32 v37, 0
	v_mov_b32_e32 v42, 0
	v_mov_b32_e32 v43, 0
	v_mfma_f32_16x16x128_f8f6f4 v[190:193], v[146:153], v[202:209], 0
	v_mov_b32_e32 v44, 0
	v_mov_b32_e32 v45, 0
	v_mov_b32_e32 v50, 0
	v_mov_b32_e32 v51, 0
	v_mfma_f32_16x16x128_f8f6f4 v[194:197], v[154:161], v[202:209], 0
	v_mov_b32_e32 v52, 0
	v_mov_b32_e32 v53, 0
	v_mov_b32_e32 v58, 0
	v_mov_b32_e32 v59, 0
	v_mfma_f32_16x16x128_f8f6f4 v[198:201], v[146:153], v[210:217], 0
	v_mov_b32_e32 v60, 0
	v_mov_b32_e32 v61, 0
	v_mov_b32_e32 v62, 0
	v_mov_b32_e32 v63, 0
	v_mfma_f32_16x16x128_f8f6f4 v[202:205], v[154:161], v[210:217], 0
	v_mov_b32_e32 v64, 0
	v_mov_b32_e32 v65, 0
	s_branch .Llzj_2

.LBB0_577:
	s_ashr_i32 s13, s12, 31
	s_lshl_b64 s[14:15], s[12:13], 18
	s_add_u32 s14, s29, s14
	s_addc_u32 s15, s30, s15
	s_and_b64 s[18:19], s[2:3], exec
	s_cselect_b32 s13, s15, s23
	s_cselect_b32 s54, s14, s22
	s_ashr_i32 s11, s10, 31
	s_lshl_b64 s[18:19], s[10:11], 18
	s_add_u32 s18, s27, s18
	s_addc_u32 s19, s28, s19
	s_and_b64 s[24:25], s[2:3], exec
	s_cselect_b32 s11, s19, s21
	s_cselect_b32 s55, s18, s20
	s_add_u32 s56, s20, 0x100
	s_addc_u32 s57, s21, 0
	s_add_u32 s20, s22, 0x80
	v_mov_b32_e32 v2, 0
	v_mov_b32_e32 v243, 1
	s_addc_u32 s21, s23, 0
	s_mov_b32 s58, -2
	v_mov_b32_e32 v3, v2
	s_branch .LBB0_578
.Llzf_3:
	v_mfma_f32_16x16x128_f8f6f4 v[126:129], v[138:145], v[170:177], 0
	v_mov_b32_e32 v4, 0
	v_mov_b32_e32 v5, 0
	v_mov_b32_e32 v6, 0
	v_mov_b32_e32 v7, 0
	v_mfma_f32_16x16x128_f8f6f4 v[122:125], v[146:153], v[170:177], 0
	v_mov_b32_e32 v8, 0
	v_mov_b32_e32 v9, 0
	v_mov_b32_e32 v10, 0
	v_mov_b32_e32 v11, 0
	v_mfma_f32_16x16x128_f8f6f4 v[118:121], v[138:145], v[186:193], 0
	v_mov_b32_e32 v12, 0
	v_mov_b32_e32 v13, 0
	v_mov_b32_e32 v18, 0
	v_mov_b32_e32 v19, 0
	v_mfma_f32_16x16x128_f8f6f4 v[110:113], v[146:153], v[186:193], 0
	v_mov_b32_e32 v20, 0
	v_mov_b32_e32 v21, 0
	v_mov_b32_e32 v26, 0
	v_mov_b32_e32 v27, 0
	v_mfma_f32_16x16x128_f8f6f4 v[102:105], v[138:145], v[194:201], 0
	v_mov_b32_e32 v28, 0
	v_mov_b32_e32 v29, 0
	v_mov_b32_e32 v34, 0
	v_mov_b32_e32 v35, 0
	v_mfma_f32_16x16x128_f8f6f4 v[178:181], v[146:153], v[194:201], 0
	v_mov_b32_e32 v36, 0
	v_mov_b32_e32 v37, 0
	v_mov_b32_e32 v42, 0
	v_mov_b32_e32 v43, 0
	v_mfma_f32_16x16x128_f8f6f4 v[210:213], v[138:145], v[202:209], 0
	v_mov_b32_e32 v44, 0
	v_mov_b32_e32 v45, 0
	v_mov_b32_e32 v50, 0
	v_mov_b32_e32 v51, 0
	v_mfma_f32_16x16x128_f8f6f4 v[214:217], v[146:153], v[202:209], 0
	v_mov_b32_e32 v52, 0
	v_mov_b32_e32 v53, 0
	v_mov_b32_e32 v14, 0
	v_mov_b32_e32 v15, 0
	s_setprio 0
	s_setprio 1
	v_mfma_f32_16x16x128_f8f6f4 v[114:117], v[154:161], v[170:177], 0
	v_mov_b32_e32 v16, 0
	v_mov_b32_e32 v17, 0
	v_mov_b32_e32 v22, 0
	v_mov_b32_e32 v23, 0
	v_mfma_f32_16x16x128_f8f6f4 v[106:109], v[162:169], v[170:177], 0
	v_mov_b32_e32 v24, 0
	v_mov_b32_e32 v25, 0
	v_mov_b32_e32 v30, 0
	v_mov_b32_e32 v31, 0
	v_mfma_f32_16x16x128_f8f6f4 v[98:101], v[154:161], v[186:193], 0
	v_mov_b32_e32 v32, 0
	v_mov_b32_e32 v33, 0
	v_mov_b32_e32 v38, 0
	v_mov_b32_e32 v39, 0
	v_mfma_f32_16x16x128_f8f6f4 v[170:173], v[162:169], v[186:193], 0
	v_mov_b32_e32 v40, 0
	v_mov_b32_e32 v41, 0
	v_mov_b32_e32 v46, 0
	v_mov_b32_e32 v47, 0
	v_mfma_f32_16x16x128_f8f6f4 v[174:177], v[154:161], v[194:201], 0
	v_mov_b32_e32 v48, 0
	v_mov_b32_e32 v49, 0
	v_mov_b32_e32 v54, 0
	v_mov_b32_e32 v55, 0
	v_mfma_f32_16x16x128_f8f6f4 v[186:189], v[162:169], v[194:201], 0
	v_mov_b32_e32 v56, 0
	v_mov_b32_e32 v57, 0
	v_mov_b32_e32 v58, 0
	v_mov_b32_e32 v59, 0
	v_mfma_f32_16x16x128_f8f6f4 v[190:193], v[154:161], v[202:209], 0
	v_mov_b32_e32 v60, 0
	v_mov_b32_e32 v61, 0
	v_mov_b32_e32 v62, 0
	v_mov_b32_e32 v63, 0
	v_mfma_f32_16x16x128_f8f6f4 v[194:197], v[162:169], v[202:209], 0
	v_mov_b32_e32 v64, 0
	v_mov_b32_e32 v65, 0
	s_branch .Llzj_3

.Llzf_4:
	v_mfma_f32_16x16x128_f8f6f4 v[126:129], v[130:137], v[186:193], 0
	v_mov_b32_e32 v4, 0
	v_mov_b32_e32 v5, 0
	v_mov_b32_e32 v6, 0
	v_mov_b32_e32 v7, 0
	v_mfma_f32_16x16x128_f8f6f4 v[122:125], v[138:145], v[186:193], 0
	v_mov_b32_e32 v8, 0
	v_mov_b32_e32 v9, 0
	v_mov_b32_e32 v14, 0
	v_mov_b32_e32 v15, 0
	v_mfma_f32_16x16x128_f8f6f4 v[110:113], v[130:137], v[194:201], 0
	v_mov_b32_e32 v16, 0
	v_mov_b32_e32 v17, 0
	v_mov_b32_e32 v22, 0
	v_mov_b32_e32 v23, 0
	v_mfma_f32_16x16x128_f8f6f4 v[106:109], v[138:145], v[194:201], 0
	v_mov_b32_e32 v24, 0
	v_mov_b32_e32 v25, 0
	v_mov_b32_e32 v30, 0
	v_mov_b32_e32 v31, 0
	v_mfma_f32_16x16x128_f8f6f4 v[98:101], v[130:137], v[202:209], 0
	v_mov_b32_e32 v32, 0
	v_mov_b32_e32 v33, 0
	v_mov_b32_e32 v38, 0
	v_mov_b32_e32 v39, 0
	v_mfma_f32_16x16x128_f8f6f4 v[162:165], v[138:145], v[202:209], 0
	v_mov_b32_e32 v40, 0
	v_mov_b32_e32 v41, 0
	v_mov_b32_e32 v46, 0
	v_mov_b32_e32 v47, 0
	v_mfma_f32_16x16x128_f8f6f4 v[172:175], v[130:137], v[210:217], 0
	v_mov_b32_e32 v48, 0
	v_mov_b32_e32 v49, 0
	v_mov_b32_e32 v54, 0
	v_mov_b32_e32 v55, 0
	v_mfma_f32_16x16x128_f8f6f4 v[176:179], v[138:145], v[210:217], 0
	v_mov_b32_e32 v56, 0
	v_mov_b32_e32 v57, 0
	v_mov_b32_e32 v10, 0
	v_mov_b32_e32 v11, 0
	s_setprio 0
	s_setprio 1
	v_mfma_f32_16x16x128_f8f6f4 v[118:121], v[146:153], v[186:193], 0
	v_mov_b32_e32 v12, 0
	v_mov_b32_e32 v13, 0
	v_mov_b32_e32 v18, 0
	v_mov_b32_e32 v19, 0
	v_mfma_f32_16x16x128_f8f6f4 v[114:117], v[154:161], v[186:193], 0
	v_mov_b32_e32 v20, 0
	v_mov_b32_e32 v21, 0
	v_mov_b32_e32 v26, 0
	v_mov_b32_e32 v27, 0
	v_mfma_f32_16x16x128_f8f6f4 v[102:105], v[146:153], v[194:201], 0
	v_mov_b32_e32 v28, 0
	v_mov_b32_e32 v29, 0
	v_mov_b32_e32 v34, 0
	v_mov_b32_e32 v35, 0
	v_mfma_f32_16x16x128_f8f6f4 v[180:183], v[154:161], v[194:201], 0
	v_mov_b32_e32 v36, 0
	v_mov_b32_e32 v37, 0
	v_mov_b32_e32 v42, 0
	v_mov_b32_e32 v43, 0
	v_mfma_f32_16x16x128_f8f6f4 v[184:187], v[146:153], v[202:209], 0
	v_mov_b32_e32 v44, 0
	v_mov_b32_e32 v45, 0
	v_mov_b32_e32 v50, 0
	v_mov_b32_e32 v51, 0
	v_mfma_f32_16x16x128_f8f6f4 v[188:191], v[154:161], v[202:209], 0
	v_mov_b32_e32 v52, 0
	v_mov_b32_e32 v53, 0
	v_mov_b32_e32 v58, 0
	v_mov_b32_e32 v59, 0
	v_mfma_f32_16x16x128_f8f6f4 v[192:195], v[146:153], v[210:217], 0
	v_mov_b32_e32 v60, 0
	v_mov_b32_e32 v61, 0
	v_mov_b32_e32 v62, 0
	v_mov_b32_e32 v63, 0
	v_mfma_f32_16x16x128_f8f6f4 v[196:199], v[154:161], v[210:217], 0
	v_mov_b32_e32 v64, 0
	v_mov_b32_e32 v65, 0
	s_branch .Llzj_4

.LBB0_1242:
	s_ashr_i32 s23, s22, 31
	s_lshl_b64 s[24:25], s[22:23], 21
	s_add_u32 s23, s1, s24
	s_addc_u32 s30, s33, s25
	s_ashr_i32 s21, s20, 31
	s_lshl_b64 s[24:25], s[20:21], 18
	s_add_u32 s24, s23, s24
	s_addc_u32 s25, s30, s25
	s_and_b64 s[30:31], s[2:3], exec
	s_cselect_b32 s21, s25, s29
	s_cselect_b32 s23, s24, s28
	s_lshl_b32 s64, s63, 10
	s_add_u32 s65, s28, 0x100
	v_mov_b32_e32 v2, 0
	s_addc_u32 s66, s29, 0
	s_mov_b32 s67, -2
	s_mov_b64 s[28:29], s[12:13]
	v_mov_b32_e32 v3, v2
	s_waitcnt vmcnt(0)
	s_xor_b32 s85, s85, 0x400
	s_cmp_eq_u32 s70, 0
	s_cbranch_scc0 .Lgb_skip
	s_load_dwordx2 s[98:99], s[96:97], 0xc0
	v_mbcnt_lo_u32_b32 v248, -1, 0
	v_mbcnt_hi_u32_b32 v248, -1, v248
	v_lshlrev_b32_e32 v248, 4, v248
	v_lshl_add_u32 v249, v66, 13, v248
	s_lshl_b32 s92, s26, 10
	v_add_u32_e32 v249, s92, v249
	s_add_i32 m0, s85, 0x26800
	s_waitcnt lgkmcnt(0)
	s_add_u32 s98, s98, s18
	s_addc_u32 s99, s99, s19
	s_nop 0
	global_load_lds_dwordx4 v249, s[98:99]

.Llzf_1:
	v_mfma_f32_16x16x128_f8f6f4 v[142:145], v[154:161], v[194:201], 0
	v_mov_b32_e32 v4, 0
	v_mov_b32_e32 v5, 0
	v_mov_b32_e32 v10, 0
	v_mov_b32_e32 v11, 0
	v_mfma_f32_16x16x128_f8f6f4 v[134:137], v[162:169], v[194:201], 0
	v_mov_b32_e32 v12, 0
	v_mov_b32_e32 v13, 0
	v_mov_b32_e32 v18, 0
	v_mov_b32_e32 v19, 0
	v_mfma_f32_16x16x128_f8f6f4 v[126:129], v[154:161], v[202:209], 0
	v_mov_b32_e32 v20, 0
	v_mov_b32_e32 v21, 0
	v_mov_b32_e32 v26, 0
	v_mov_b32_e32 v27, 0
	v_mfma_f32_16x16x128_f8f6f4 v[118:121], v[162:169], v[202:209], 0
	v_mov_b32_e32 v28, 0
	v_mov_b32_e32 v29, 0
	v_mov_b32_e32 v34, 0
	v_mov_b32_e32 v35, 0
	v_mfma_f32_16x16x128_f8f6f4 v[110:113], v[154:161], v[210:217], 0
	v_mov_b32_e32 v36, 0
	v_mov_b32_e32 v37, 0
	v_mov_b32_e32 v42, 0
	v_mov_b32_e32 v43, 0
	v_mfma_f32_16x16x128_f8f6f4 v[102:105], v[162:169], v[210:217], 0
	v_mov_b32_e32 v44, 0
	v_mov_b32_e32 v45, 0
	v_mov_b32_e32 v50, 0
	v_mov_b32_e32 v51, 0
	v_mfma_f32_16x16x128_f8f6f4 v[178:181], v[154:161], v[244:251], 0
	v_mov_b32_e32 v52, 0
	v_mov_b32_e32 v53, 0
	v_mov_b32_e32 v58, 0
	v_mov_b32_e32 v59, 0
	v_mfma_f32_16x16x128_f8f6f4 v[182:185], v[162:169], v[244:251], 0
	v_mov_b32_e32 v60, 0
	v_mov_b32_e32 v61, 0
	v_mov_b32_e32 v6, 0
	v_mov_b32_e32 v7, 0
	s_setprio 0
	s_setprio 1
	v_mfma_f32_16x16x128_f8f6f4 v[138:141], v[170:177], v[194:201], 0
	v_mov_b32_e32 v8, 0
	v_mov_b32_e32 v9, 0
	v_mov_b32_e32 v14, 0
	v_mov_b32_e32 v15, 0
	v_mfma_f32_16x16x128_f8f6f4 v[130:133], v[186:193], v[194:201], 0
	v_mov_b32_e32 v16, 0
	v_mov_b32_e32 v17, 0
	v_mov_b32_e32 v22, 0
	v_mov_b32_e32 v23, 0
	v_mfma_f32_16x16x128_f8f6f4 v[122:125], v[170:177], v[202:209], 0
	v_mov_b32_e32 v24, 0
	v_mov_b32_e32 v25, 0
	v_mov_b32_e32 v30, 0
	v_mov_b32_e32 v31, 0
	v_mfma_f32_16x16x128_f8f6f4 v[114:117], v[186:193], v[202:209], 0
	v_mov_b32_e32 v32, 0
	v_mov_b32_e32 v33, 0
	v_mov_b32_e32 v38, 0
	v_mov_b32_e32 v39, 0
	v_mfma_f32_16x16x128_f8f6f4 v[106:109], v[170:177], v[210:217], 0
	v_mov_b32_e32 v40, 0
	v_mov_b32_e32 v41, 0
	v_mov_b32_e32 v46, 0
	v_mov_b32_e32 v47, 0
	v_mfma_f32_16x16x128_f8f6f4 v[194:197], v[186:193], v[210:217], 0
	v_mov_b32_e32 v48, 0
	v_mov_b32_e32 v49, 0
	v_mov_b32_e32 v54, 0
	v_mov_b32_e32 v55, 0
	v_mfma_f32_16x16x128_f8f6f4 v[198:201], v[170:177], v[244:251], 0
	v_mov_b32_e32 v56, 0
	v_mov_b32_e32 v57, 0
	v_mov_b32_e32 v62, 0
	v_mov_b32_e32 v63, 0
	v_mfma_f32_16x16x128_f8f6f4 v[202:205], v[186:193], v[244:251], 0
	v_mov_b32_e32 v64, 0
	v_mov_b32_e32 v65, 0
	s_branch .Llzj_1

.LBB0_1348:
	s_ashr_i32 s15, s14, 31
	s_lshl_b64 s[18:19], s[14:15], 18
	s_add_u32 s18, s40, s18
	s_addc_u32 s19, s41, s19
	s_and_b64 s[20:21], s[2:3], exec
	s_cselect_b32 s15, s19, s29
	s_cselect_b32 s64, s18, s28
	s_ashr_i32 s17, s16, 31
	s_lshl_b64 s[20:21], s[16:17], 20
	s_add_u32 s17, s42, s20
	s_addc_u32 s30, s43, s21
	s_ashr_i32 s13, s12, 31
	s_lshl_b64 s[20:21], s[12:13], 18
	s_add_u32 s20, s17, s20
	s_addc_u32 s21, s30, s21
	s_and_b64 s[30:31], s[2:3], exec
	s_cselect_b32 s13, s21, s27
	s_cselect_b32 s17, s20, s26
	s_add_u32 s65, s26, 0x100
	s_addc_u32 s66, s27, 0
	s_add_u32 s26, s28, 0x80
	v_mov_b32_e32 v2, 0
	s_addc_u32 s27, s29, 0
	s_mov_b32 s67, -2
	v_mov_b32_e32 v3, v2
	s_waitcnt vmcnt(0)
	s_branch .LBB0_1349
.Llzf_0:
	v_mfma_f32_16x16x128_f8f6f4 v[126:129], v[132:139], v[186:193], 0
	v_mov_b32_e32 v4, 0
	v_mov_b32_e32 v5, 0
	v_mov_b32_e32 v6, 0
	v_mov_b32_e32 v7, 0
	v_mfma_f32_16x16x128_f8f6f4 v[122:125], v[140:147], v[186:193], 0
	v_mov_b32_e32 v8, 0
	v_mov_b32_e32 v9, 0
	v_mov_b32_e32 v10, 0
	v_mov_b32_e32 v11, 0
	v_mfma_f32_16x16x128_f8f6f4 v[118:121], v[132:139], v[194:201], 0
	v_mov_b32_e32 v12, 0
	v_mov_b32_e32 v13, 0
	v_mov_b32_e32 v14, 0
	v_mov_b32_e32 v15, 0
	v_mfma_f32_16x16x128_f8f6f4 v[114:117], v[140:147], v[194:201], 0
	v_mov_b32_e32 v16, 0
	v_mov_b32_e32 v17, 0
	v_mov_b32_e32 v18, 0
	v_mov_b32_e32 v19, 0
	v_mfma_f32_16x16x128_f8f6f4 v[110:113], v[132:139], v[202:209], 0
	v_mov_b32_e32 v20, 0
	v_mov_b32_e32 v21, 0
	v_mov_b32_e32 v22, 0
	v_mov_b32_e32 v23, 0
	v_mfma_f32_16x16x128_f8f6f4 v[106:109], v[140:147], v[202:209], 0
	v_mov_b32_e32 v24, 0
	v_mov_b32_e32 v25, 0
	v_mov_b32_e32 v26, 0
	v_mov_b32_e32 v27, 0
	v_mfma_f32_16x16x128_f8f6f4 v[172:175], v[132:139], v[210:217], 0
	v_mov_b32_e32 v28, 0
	v_mov_b32_e32 v29, 0
	v_mov_b32_e32 v30, 0
	v_mov_b32_e32 v31, 0
	v_mfma_f32_16x16x128_f8f6f4 v[176:179], v[140:147], v[210:217], 0
	v_mov_b32_e32 v32, 0
	v_mov_b32_e32 v33, 0
	v_mov_b32_e32 v58, 0
	v_mov_b32_e32 v59, 0
	s_setprio 0
	s_setprio 1
	v_mfma_f32_16x16x128_f8f6f4 v[70:73], v[148:155], v[186:193], 0
	v_mov_b32_e32 v60, 0
	v_mov_b32_e32 v61, 0
	v_mov_b32_e32 v66, 0
	v_mov_b32_e32 v67, 0
	v_mfma_f32_16x16x128_f8f6f4 v[62:65], v[156:163], v[186:193], 0
	v_mov_b32_e32 v68, 0
	v_mov_b32_e32 v69, 0
	v_mov_b32_e32 v74, 0
	v_mov_b32_e32 v75, 0
	v_mfma_f32_16x16x128_f8f6f4 v[180:183], v[148:155], v[194:201], 0
	v_mov_b32_e32 v76, 0
	v_mov_b32_e32 v77, 0
	v_mov_b32_e32 v78, 0
	v_mov_b32_e32 v79, 0
	v_mfma_f32_16x16x128_f8f6f4 v[184:187], v[156:163], v[194:201], 0
	v_mov_b32_e32 v80, 0
	v_mov_b32_e32 v81, 0
	v_mov_b32_e32 v82, 0
	v_mov_b32_e32 v83, 0
	v_mfma_f32_16x16x128_f8f6f4 v[188:191], v[148:155], v[202:209], 0
	v_mov_b32_e32 v84, 0
	v_mov_b32_e32 v85, 0
	v_mov_b32_e32 v86, 0
	v_mov_b32_e32 v87, 0
	v_mfma_f32_16x16x128_f8f6f4 v[192:195], v[156:163], v[202:209], 0
	v_mov_b32_e32 v88, 0
	v_mov_b32_e32 v89, 0
	v_mov_b32_e32 v90, 0
	v_mov_b32_e32 v91, 0
	v_mfma_f32_16x16x128_f8f6f4 v[196:199], v[148:155], v[210:217], 0
	v_mov_b32_e32 v92, 0
	v_mov_b32_e32 v93, 0
	v_mov_b32_e32 v94, 0
	v_mov_b32_e32 v95, 0
	v_mfma_f32_16x16x128_f8f6f4 v[200:203], v[156:163], v[210:217], 0
	v_mov_b32_e32 v96, 0
	v_mov_b32_e32 v97, 0
	s_branch .Llzj_0
